# MLP1 K-loop: loop-invariant M0 bases and ds_read base addresses hoisted out of the loop (on v40)
# speedup vs baseline: 1.0177x; 1.0111x over previous
.LBB5_53:
	v_mov_b32_e32 v95, 0
	s_andn2_b64 vcc, exec, s[24:25]
	v_mov_b32_e32 v94, v95
	v_mov_b32_e32 v93, v95
	v_mov_b32_e32 v92, v95
	v_mov_b32_e32 v91, v95
	v_mov_b32_e32 v90, v95
	v_mov_b32_e32 v89, v95
	v_mov_b32_e32 v88, v95
	v_mov_b32_e32 v79, v95
	v_mov_b32_e32 v78, v95
	v_mov_b32_e32 v77, v95
	v_mov_b32_e32 v76, v95
	v_mov_b32_e32 v75, v95
	v_mov_b32_e32 v74, v95
	v_mov_b32_e32 v73, v95
	v_mov_b32_e32 v72, v95
	v_mov_b32_e32 v31, v95
	v_mov_b32_e32 v30, v95
	v_mov_b32_e32 v29, v95
	v_mov_b32_e32 v28, v95
	v_mov_b32_e32 v27, v95
	v_mov_b32_e32 v26, v95
	v_mov_b32_e32 v25, v95
	v_mov_b32_e32 v24, v95
	v_mov_b32_e32 v15, v95
	v_mov_b32_e32 v14, v95
	v_mov_b32_e32 v13, v95
	v_mov_b32_e32 v12, v95
	v_mov_b32_e32 v11, v95
	v_mov_b32_e32 v10, v95
	v_mov_b32_e32 v9, v95
	v_mov_b32_e32 v8, v95
	v_mov_b32_e32 v87, v95
	v_mov_b32_e32 v86, v95
	v_mov_b32_e32 v85, v95
	v_mov_b32_e32 v84, v95
	v_mov_b32_e32 v83, v95
	v_mov_b32_e32 v82, v95
	v_mov_b32_e32 v81, v95
	v_mov_b32_e32 v80, v95
	v_mov_b32_e32 v55, v95
	v_mov_b32_e32 v54, v95
	v_mov_b32_e32 v53, v95
	v_mov_b32_e32 v52, v95
	v_mov_b32_e32 v51, v95
	v_mov_b32_e32 v50, v95
	v_mov_b32_e32 v49, v95
	v_mov_b32_e32 v48, v95
	v_mov_b32_e32 v23, v95
	v_mov_b32_e32 v22, v95
	v_mov_b32_e32 v21, v95
	v_mov_b32_e32 v20, v95
	v_mov_b32_e32 v19, v95
	v_mov_b32_e32 v18, v95
	v_mov_b32_e32 v17, v95
	v_mov_b32_e32 v16, v95
	v_mov_b32_e32 v7, v95
	v_mov_b32_e32 v6, v95
	v_mov_b32_e32 v5, v95
	v_mov_b32_e32 v4, v95
	v_mov_b32_e32 v3, v95
	v_mov_b32_e32 v2, v95
	v_mov_b32_e32 v1, v95
	v_mov_b32_e32 v0, v95
	s_cbranch_vccnz .LBB5_42
	v_mov_b32_e32 v0, 0
	v_lshl_add_u64 v[32:33], s[40:41], 0, v[112:113]
	v_lshl_add_u64 v[34:35], s[40:41], 0, v[114:115]
	v_lshl_add_u64 v[36:37], s[42:43], 0, v[116:117]
	v_lshl_add_u64 v[38:39], s[42:43], 0, v[118:119]
	v_lshl_add_u64 v[40:41], s[42:43], 0, v[120:121]
	v_lshl_add_u64 v[42:43], s[42:43], 0, v[122:123]
	s_mov_b32 s75, 0
	s_mov_b64 s[44:45], 0
	v_mov_b32_e32 v1, v0
	v_mov_b32_e32 v2, v0
	v_mov_b32_e32 v3, v0
	v_mov_b32_e32 v4, v0
	v_mov_b32_e32 v5, v0
	v_mov_b32_e32 v6, v0
	v_mov_b32_e32 v7, v0
	v_mov_b32_e32 v16, v0
	v_mov_b32_e32 v17, v0
	v_mov_b32_e32 v18, v0
	v_mov_b32_e32 v19, v0
	v_mov_b32_e32 v20, v0
	v_mov_b32_e32 v21, v0
	v_mov_b32_e32 v22, v0
	v_mov_b32_e32 v23, v0
	v_mov_b32_e32 v48, v0
	v_mov_b32_e32 v49, v0
	v_mov_b32_e32 v50, v0
	v_mov_b32_e32 v51, v0
	v_mov_b32_e32 v52, v0
	v_mov_b32_e32 v53, v0
	v_mov_b32_e32 v54, v0
	v_mov_b32_e32 v55, v0
	v_mov_b32_e32 v80, v0
	v_mov_b32_e32 v81, v0
	v_mov_b32_e32 v82, v0
	v_mov_b32_e32 v83, v0
	v_mov_b32_e32 v84, v0
	v_mov_b32_e32 v85, v0
	v_mov_b32_e32 v86, v0
	v_mov_b32_e32 v87, v0
	v_mov_b32_e32 v8, v0
	v_mov_b32_e32 v9, v0
	v_mov_b32_e32 v10, v0
	v_mov_b32_e32 v11, v0
	v_mov_b32_e32 v12, v0
	v_mov_b32_e32 v13, v0
	v_mov_b32_e32 v14, v0
	v_mov_b32_e32 v15, v0
	v_mov_b32_e32 v24, v0
	v_mov_b32_e32 v25, v0
	v_mov_b32_e32 v26, v0
	v_mov_b32_e32 v27, v0
	v_mov_b32_e32 v28, v0
	v_mov_b32_e32 v29, v0
	v_mov_b32_e32 v30, v0
	v_mov_b32_e32 v31, v0
	v_mov_b32_e32 v72, v0
	v_mov_b32_e32 v73, v0
	v_mov_b32_e32 v74, v0
	v_mov_b32_e32 v75, v0
	v_mov_b32_e32 v76, v0
	v_mov_b32_e32 v77, v0
	v_mov_b32_e32 v78, v0
	v_mov_b32_e32 v79, v0
	v_mov_b32_e32 v88, v0
	v_mov_b32_e32 v89, v0
	v_mov_b32_e32 v90, v0
	v_mov_b32_e32 v91, v0
	v_mov_b32_e32 v92, v0
	v_mov_b32_e32 v93, v0
	v_mov_b32_e32 v94, v0
	v_mov_b32_e32 v95, v0
	s_add_u32 s78, s40, s44
	s_addc_u32 s79, s41, s45
	s_add_u32 s80, s42, s44
	s_addc_u32 s81, s43, s45
	s_add_u32 s46, s40, s44
	s_addc_u32 s47, s41, s45
	s_add_u32 s46, s46, 0x180
	s_addc_u32 s47, s47, 0
	s_add_u32 s48, s42, s44
	s_addc_u32 s49, s43, s45
	s_add_u32 s76, s48, 0x180
	s_addc_u32 s77, s49, 0
	s_cmp_eq_u32 s67, s75
	s_cselect_b32 s49, s7, s47
	s_cselect_b32 s48, s6, s46
	s_cselect_b32 s47, s5, s77
	s_cselect_b32 s46, s4, s76
	s_add_u32 s82, s48, 0x80
	s_addc_u32 s83, s49, 0
	s_add_u32 s84, s46, 0x80
	s_addc_u32 s85, s47, 0
	s_add_u32 s86, s84, s10
	s_addc_u32 s87, s85, s11
	s_add_i32 s76, s19, s54
	s_add_i32 s88, s27, s54
	s_add_i32 s89, s68, s54
	s_add_i32 s90, s54, 0x10000
	s_add_i32 s91, s54, 0x14000
	v_add_u32_e32 v170, 0x10000, v128
	v_add_u32_e32 v171, 0x14000, v128
.LBB5_55:
	s_mov_b32 m0, s76
	ds_read_b128 v[44:47], v130 offset:16384
	ds_read_b128 v[56:59], v130 offset:17408
	ds_read_b128 v[60:63], v130 offset:18432
	ds_read_b128 v[64:67], v130 offset:19456
	ds_read_b128 v[68:71], v131
	ds_read_b128 v[96:99], v131 offset:1024
	ds_read_b128 v[136:139], v131 offset:2048
	ds_read_b128 v[140:143], v131 offset:3072
	ds_read_b128 v[144:147], v131 offset:4096
	ds_read_b128 v[148:151], v131 offset:5120
	ds_read_b128 v[152:155], v131 offset:6144
	ds_read_b128 v[156:159], v131 offset:7168
	global_load_lds_dwordx4 v112, s[78:79]
	s_add_i32 m0, s76, 0x2000
	s_nop 0
	global_load_lds_dwordx4 v114, s[78:79]
	s_mov_b32 m0, s88
	s_nop 0
	global_load_lds_dwordx4 v116, s[80:81]
	s_add_i32 m0, s88, 0x2000
	s_nop 0
	global_load_lds_dwordx4 v118, s[80:81]
	s_barrier
	s_setprio 1
	s_waitcnt lgkmcnt(7)
	v_mfma_f32_16x16x32_f16 v[92:95], v[44:47], v[68:71], v[92:95]
	v_mfma_f32_16x16x32_f16 v[88:91], v[60:63], v[68:71], v[88:91]
	s_waitcnt lgkmcnt(5)
	v_mfma_f32_16x16x32_f16 v[76:79], v[44:47], v[136:139], v[76:79]
	v_mfma_f32_16x16x32_f16 v[72:75], v[60:63], v[136:139], v[72:75]
	s_waitcnt lgkmcnt(3)
	v_mfma_f32_16x16x32_f16 v[28:31], v[44:47], v[144:147], v[28:31]
	v_mfma_f32_16x16x32_f16 v[24:27], v[60:63], v[144:147], v[24:27]
	s_waitcnt lgkmcnt(1)
	v_mfma_f32_16x16x32_f16 v[12:15], v[44:47], v[152:155], v[12:15]
	v_mfma_f32_16x16x32_f16 v[8:11], v[60:63], v[152:155], v[8:11]
	v_mfma_f32_16x16x32_f16 v[92:95], v[56:59], v[96:99], v[92:95]
	v_mfma_f32_16x16x32_f16 v[88:91], v[64:67], v[96:99], v[88:91]
	v_mfma_f32_16x16x32_f16 v[76:79], v[56:59], v[140:143], v[76:79]
	v_mfma_f32_16x16x32_f16 v[72:75], v[64:67], v[140:143], v[72:75]
	v_mfma_f32_16x16x32_f16 v[28:31], v[56:59], v[148:151], v[28:31]
	v_mfma_f32_16x16x32_f16 v[24:27], v[64:67], v[148:151], v[24:27]
	s_waitcnt lgkmcnt(0)
	v_mfma_f32_16x16x32_f16 v[12:15], v[56:59], v[156:159], v[12:15]
	v_mfma_f32_16x16x32_f16 v[8:11], v[64:67], v[156:159], v[8:11]
	s_setprio 0
	s_barrier
	s_mov_b32 m0, s89
	ds_read_b128 v[44:47], v130 offset:32768
	ds_read_b128 v[56:59], v130 offset:33792
	ds_read_b128 v[60:63], v130 offset:34816
	ds_read_b128 v[64:67], v130 offset:35840
	global_load_lds_dwordx4 v120, s[80:81]
	s_add_i32 m0, s89, 0x2000
	s_nop 0
	global_load_lds_dwordx4 v122, s[80:81]
	s_waitcnt vmcnt(6)
	s_barrier
	s_setprio 1
	s_waitcnt lgkmcnt(3)
	v_mfma_f32_16x16x32_f16 v[84:87], v[44:47], v[68:71], v[84:87]
	v_mfma_f32_16x16x32_f16 v[52:55], v[44:47], v[136:139], v[52:55]
	s_waitcnt lgkmcnt(1)
	v_mfma_f32_16x16x32_f16 v[48:51], v[60:63], v[136:139], v[48:51]
	v_mfma_f32_16x16x32_f16 v[20:23], v[44:47], v[144:147], v[20:23]
	v_mfma_f32_16x16x32_f16 v[16:19], v[60:63], v[144:147], v[16:19]
	v_mfma_f32_16x16x32_f16 v[4:7], v[44:47], v[152:155], v[4:7]
	v_mfma_f32_16x16x32_f16 v[0:3], v[60:63], v[152:155], v[0:3]
	v_mfma_f32_16x16x32_f16 v[84:87], v[56:59], v[96:99], v[84:87]
	v_mfma_f32_16x16x32_f16 v[68:71], v[60:63], v[68:71], v[80:83]
	v_mfma_f32_16x16x32_f16 v[52:55], v[56:59], v[140:143], v[52:55]
	s_waitcnt lgkmcnt(0)
	v_mfma_f32_16x16x32_f16 v[48:51], v[64:67], v[140:143], v[48:51]
	v_mfma_f32_16x16x32_f16 v[20:23], v[56:59], v[148:151], v[20:23]
	v_mfma_f32_16x16x32_f16 v[16:19], v[64:67], v[148:151], v[16:19]
	v_mfma_f32_16x16x32_f16 v[4:7], v[56:59], v[156:159], v[4:7]
	v_mfma_f32_16x16x32_f16 v[0:3], v[64:67], v[156:159], v[0:3]
	v_mfma_f32_16x16x32_f16 v[68:71], v[64:67], v[96:99], v[68:71]
	s_setprio 0
	s_barrier
	s_mov_b32 m0, s57
	ds_read_b128 v[44:47], v170
	ds_read_b128 v[56:59], v170 offset:1024
	ds_read_b128 v[60:63], v170 offset:2048
	ds_read_b128 v[64:67], v170 offset:3072
	ds_read_b128 v[80:83], v131 offset:49152
	ds_read_b128 v[96:99], v131 offset:50176
	ds_read_b128 v[136:139], v131 offset:51200
	ds_read_b128 v[140:143], v131 offset:52224
	ds_read_b128 v[144:147], v131 offset:53248
	ds_read_b128 v[148:151], v131 offset:54272
	ds_read_b128 v[152:155], v131 offset:55296
	ds_read_b128 v[156:159], v131 offset:56320
	global_load_lds_dwordx4 v100, s[48:49]
	s_mov_b32 m0, s58
	s_nop 0
	global_load_lds_dwordx4 v104, s[48:49]
	s_mov_b32 m0, s59
	s_nop 0
	global_load_lds_dwordx4 v102, s[46:47]
	s_mov_b32 m0, s60
	s_nop 0
	global_load_lds_dwordx4 v106, s[46:47]
	s_barrier
	s_setprio 1
	s_waitcnt lgkmcnt(7)
	v_mfma_f32_16x16x32_f16 v[92:95], v[44:47], v[80:83], v[92:95]
	v_mfma_f32_16x16x32_f16 v[88:91], v[60:63], v[80:83], v[88:91]
	s_waitcnt lgkmcnt(5)
	v_mfma_f32_16x16x32_f16 v[76:79], v[44:47], v[136:139], v[76:79]
	v_mfma_f32_16x16x32_f16 v[72:75], v[60:63], v[136:139], v[72:75]
	s_waitcnt lgkmcnt(3)
	v_mfma_f32_16x16x32_f16 v[28:31], v[44:47], v[144:147], v[28:31]
	v_mfma_f32_16x16x32_f16 v[24:27], v[60:63], v[144:147], v[24:27]
	s_waitcnt lgkmcnt(1)
	v_mfma_f32_16x16x32_f16 v[12:15], v[44:47], v[152:155], v[12:15]
	v_mfma_f32_16x16x32_f16 v[8:11], v[60:63], v[152:155], v[8:11]
	v_mfma_f32_16x16x32_f16 v[92:95], v[56:59], v[96:99], v[92:95]
	v_mfma_f32_16x16x32_f16 v[88:91], v[64:67], v[96:99], v[88:91]
	v_mfma_f32_16x16x32_f16 v[76:79], v[56:59], v[140:143], v[76:79]
	v_mfma_f32_16x16x32_f16 v[72:75], v[64:67], v[140:143], v[72:75]
	v_mfma_f32_16x16x32_f16 v[28:31], v[56:59], v[148:151], v[28:31]
	v_mfma_f32_16x16x32_f16 v[24:27], v[64:67], v[148:151], v[24:27]
	s_waitcnt lgkmcnt(0)
	v_mfma_f32_16x16x32_f16 v[12:15], v[56:59], v[156:159], v[12:15]
	v_mfma_f32_16x16x32_f16 v[8:11], v[64:67], v[156:159], v[8:11]
	s_setprio 0
	s_barrier
	s_add_u32 s46, s46, s10
	s_addc_u32 s47, s47, s11
	s_mov_b32 m0, s61
	ds_read_b128 v[44:47], v171
	ds_read_b128 v[56:59], v171 offset:1024
	ds_read_b128 v[60:63], v171 offset:2048
	ds_read_b128 v[64:67], v171 offset:3072
	global_load_lds_dwordx4 v102, s[46:47]
	s_mov_b32 m0, s62
	s_nop 0
	global_load_lds_dwordx4 v106, s[46:47]
	s_waitcnt vmcnt(6)
	s_barrier
	s_setprio 1
	s_waitcnt lgkmcnt(3)
	v_mfma_f32_16x16x32_f16 v[84:87], v[44:47], v[80:83], v[84:87]
	v_mfma_f32_16x16x32_f16 v[52:55], v[44:47], v[136:139], v[52:55]
	s_waitcnt lgkmcnt(1)
	v_mfma_f32_16x16x32_f16 v[48:51], v[60:63], v[136:139], v[48:51]
	v_mfma_f32_16x16x32_f16 v[20:23], v[44:47], v[144:147], v[20:23]
	v_mfma_f32_16x16x32_f16 v[16:19], v[60:63], v[144:147], v[16:19]
	v_mfma_f32_16x16x32_f16 v[4:7], v[44:47], v[152:155], v[4:7]
	v_mfma_f32_16x16x32_f16 v[0:3], v[60:63], v[152:155], v[0:3]
	v_mfma_f32_16x16x32_f16 v[84:87], v[56:59], v[96:99], v[84:87]
	v_mfma_f32_16x16x32_f16 v[68:71], v[60:63], v[80:83], v[68:71]
	v_mfma_f32_16x16x32_f16 v[52:55], v[56:59], v[140:143], v[52:55]
	s_waitcnt lgkmcnt(0)
	v_mfma_f32_16x16x32_f16 v[48:51], v[64:67], v[140:143], v[48:51]
	v_mfma_f32_16x16x32_f16 v[20:23], v[56:59], v[148:151], v[20:23]
	v_mfma_f32_16x16x32_f16 v[16:19], v[64:67], v[148:151], v[16:19]
	v_mfma_f32_16x16x32_f16 v[4:7], v[56:59], v[156:159], v[4:7]
	v_mfma_f32_16x16x32_f16 v[0:3], v[64:67], v[156:159], v[0:3]
	v_mfma_f32_16x16x32_f16 v[68:71], v[64:67], v[96:99], v[68:71]
	s_setprio 0
	s_barrier
	s_mov_b32 m0, s64
	ds_read_b128 v[44:47], v132
	ds_read_b128 v[56:59], v132 offset:1024
	ds_read_b128 v[60:63], v132 offset:2048
	ds_read_b128 v[64:67], v132 offset:3072
	ds_read_b128 v[80:83], v133
	ds_read_b128 v[96:99], v133 offset:1024
	ds_read_b128 v[136:139], v133 offset:2048
	ds_read_b128 v[140:143], v133 offset:3072
	ds_read_b128 v[144:147], v133 offset:4096
	ds_read_b128 v[148:151], v133 offset:5120
	ds_read_b128 v[152:155], v133 offset:6144
	ds_read_b128 v[156:159], v133 offset:7168
	global_load_lds_dwordx4 v100, s[82:83]
	s_mov_b32 m0, s65
	s_nop 0
	global_load_lds_dwordx4 v104, s[82:83]
	s_mov_b32 m0, s90
	s_nop 0
	global_load_lds_dwordx4 v102, s[84:85]
	s_add_i32 m0, s90, 0x2000
	s_nop 0
	global_load_lds_dwordx4 v106, s[84:85]
	s_barrier
	s_setprio 1
	s_waitcnt lgkmcnt(7)
	v_mfma_f32_16x16x32_f16 v[92:95], v[44:47], v[80:83], v[92:95]
	v_mfma_f32_16x16x32_f16 v[88:91], v[60:63], v[80:83], v[88:91]
	s_waitcnt lgkmcnt(5)
	v_mfma_f32_16x16x32_f16 v[76:79], v[44:47], v[136:139], v[76:79]
	v_mfma_f32_16x16x32_f16 v[72:75], v[60:63], v[136:139], v[72:75]
	s_waitcnt lgkmcnt(3)
	v_mfma_f32_16x16x32_f16 v[28:31], v[44:47], v[144:147], v[28:31]
	v_mfma_f32_16x16x32_f16 v[24:27], v[60:63], v[144:147], v[24:27]
	s_waitcnt lgkmcnt(1)
	v_mfma_f32_16x16x32_f16 v[12:15], v[44:47], v[152:155], v[12:15]
	v_mfma_f32_16x16x32_f16 v[8:11], v[60:63], v[152:155], v[8:11]
	v_mfma_f32_16x16x32_f16 v[92:95], v[56:59], v[96:99], v[92:95]
	v_mfma_f32_16x16x32_f16 v[88:91], v[64:67], v[96:99], v[88:91]
	v_mfma_f32_16x16x32_f16 v[76:79], v[56:59], v[140:143], v[76:79]
	v_mfma_f32_16x16x32_f16 v[72:75], v[64:67], v[140:143], v[72:75]
	v_mfma_f32_16x16x32_f16 v[28:31], v[56:59], v[148:151], v[28:31]
	v_mfma_f32_16x16x32_f16 v[24:27], v[64:67], v[148:151], v[24:27]
	s_waitcnt lgkmcnt(0)
	v_mfma_f32_16x16x32_f16 v[12:15], v[56:59], v[156:159], v[12:15]
	v_mfma_f32_16x16x32_f16 v[8:11], v[64:67], v[156:159], v[8:11]
	s_setprio 0
	s_barrier
	s_mov_b32 m0, s91
	ds_read_b128 v[44:47], v134
	ds_read_b128 v[56:59], v134 offset:1024
	ds_read_b128 v[60:63], v134 offset:2048
	ds_read_b128 v[64:67], v134 offset:3072
	global_load_lds_dwordx4 v102, s[86:87]
	s_add_i32 m0, s91, 0x2000
	s_nop 0
	global_load_lds_dwordx4 v106, s[86:87]
	s_waitcnt vmcnt(6)
	s_barrier
	s_setprio 1
	s_waitcnt lgkmcnt(3)
	v_mfma_f32_16x16x32_f16 v[84:87], v[44:47], v[80:83], v[84:87]
	s_waitcnt lgkmcnt(1)
	v_mfma_f32_16x16x32_f16 v[68:71], v[60:63], v[80:83], v[68:71]
	v_mfma_f32_16x16x32_f16 v[52:55], v[44:47], v[136:139], v[52:55]
	v_mfma_f32_16x16x32_f16 v[48:51], v[60:63], v[136:139], v[48:51]
	v_mfma_f32_16x16x32_f16 v[20:23], v[44:47], v[144:147], v[20:23]
	v_mfma_f32_16x16x32_f16 v[16:19], v[60:63], v[144:147], v[16:19]
	v_mfma_f32_16x16x32_f16 v[4:7], v[44:47], v[152:155], v[4:7]
	v_mfma_f32_16x16x32_f16 v[0:3], v[60:63], v[152:155], v[0:3]
	v_mfma_f32_16x16x32_f16 v[84:87], v[56:59], v[96:99], v[84:87]
	s_waitcnt lgkmcnt(0)
	v_mfma_f32_16x16x32_f16 v[80:83], v[64:67], v[96:99], v[68:71]
	v_mfma_f32_16x16x32_f16 v[52:55], v[56:59], v[140:143], v[52:55]
	v_mfma_f32_16x16x32_f16 v[48:51], v[64:67], v[140:143], v[48:51]
	v_mfma_f32_16x16x32_f16 v[20:23], v[56:59], v[148:151], v[20:23]
	v_mfma_f32_16x16x32_f16 v[16:19], v[64:67], v[148:151], v[16:19]
	v_mfma_f32_16x16x32_f16 v[4:7], v[56:59], v[156:159], v[4:7]
	v_mfma_f32_16x16x32_f16 v[0:3], v[64:67], v[156:159], v[0:3]
	s_setprio 0
	s_add_i32 s75, s75, 3
	s_add_u32 s44, s44, 0x180
	s_addc_u32 s45, s45, 0
	s_cmp_ge_i32 s75, s66
	s_cbranch_scc1 .Lrot_exit_mlp1
	s_add_u32 s78, s40, s44
	s_addc_u32 s79, s41, s45
	s_add_u32 s80, s42, s44
	s_addc_u32 s81, s43, s45
	s_add_u32 s46, s40, s44
	s_addc_u32 s47, s41, s45
	s_add_u32 s46, s46, 0x180
	s_addc_u32 s47, s47, 0
	s_add_u32 s48, s42, s44
	s_addc_u32 s49, s43, s45
	s_add_u32 s76, s48, 0x180
	s_addc_u32 s77, s49, 0
	s_cmp_eq_u32 s67, s75
	s_cselect_b32 s49, s7, s47
	s_cselect_b32 s48, s6, s46
	s_cselect_b32 s47, s5, s77
	s_cselect_b32 s46, s4, s76
	s_add_u32 s82, s48, 0x80
	s_addc_u32 s83, s49, 0
	s_add_u32 s84, s46, 0x80
	s_addc_u32 s85, s47, 0
	s_add_u32 s86, s84, s10
	s_addc_u32 s87, s85, s11
	s_add_i32 s76, s19, s54
	s_barrier
	s_branch .LBB5_55

	.amdhsa_kernel _Z9k_gemm128IN4g1289EpiGeluLNEEvNS0_4GemmET_
		.amdhsa_group_segment_fixed_size 0
		.amdhsa_private_segment_fixed_size 0
		.amdhsa_kernarg_size 344
		.amdhsa_user_sgpr_count 2
		.amdhsa_user_sgpr_dispatch_ptr 0
		.amdhsa_user_sgpr_queue_ptr 0
		.amdhsa_user_sgpr_kernarg_segment_ptr 1
		.amdhsa_user_sgpr_dispatch_id 0
		.amdhsa_user_sgpr_kernarg_preload_length 0
		.amdhsa_user_sgpr_kernarg_preload_offset 0
		.amdhsa_user_sgpr_private_segment_size 0
		.amdhsa_uses_dynamic_stack 0
		.amdhsa_enable_private_segment 0
		.amdhsa_system_sgpr_workgroup_id_x 1
		.amdhsa_system_sgpr_workgroup_id_y 0
		.amdhsa_system_sgpr_workgroup_id_z 0
		.amdhsa_system_sgpr_workgroup_info 0
		.amdhsa_system_vgpr_workitem_id 0
		.amdhsa_next_free_vgpr 172
		.amdhsa_next_free_sgpr 92
		.amdhsa_accum_offset 172
		.amdhsa_reserve_vcc 1
		.amdhsa_float_round_mode_32 0
		.amdhsa_float_round_mode_16_64 0
		.amdhsa_float_denorm_mode_32 3
		.amdhsa_float_denorm_mode_16_64 3
		.amdhsa_dx10_clamp 1
		.amdhsa_ieee_mode 1
		.amdhsa_fp16_overflow 0
		.amdhsa_tg_split 0
		.amdhsa_exception_fp_ieee_invalid_op 0
		.amdhsa_exception_fp_denorm_src 0
		.amdhsa_exception_fp_ieee_div_zero 0
		.amdhsa_exception_fp_ieee_overflow 0
		.amdhsa_exception_fp_ieee_underflow 0
		.amdhsa_exception_fp_ieee_inexact 0
		.amdhsa_exception_int_div_zero 0
	.end_amdhsa_kernel
